# speedup vs baseline: 1.0095x; 1.0018x over previous
.Llight_path:
	s_waitcnt vmcnt(16)
	v_mul_u32_u24_e32 v236, 36, v228
	v_add_u32_e32 v236, v236, v230
	v_add_u32_e32 v237, s7, v229
	v_mul_u32_u24_e32 v238, 0x104, v228
	v_add_u32_e32 v238, v238, v237
	v_add_u32_e32 v238, 0xb840, v238
	v_add_u32_e32 v231, s7, v229
	v_add_u32_e32 v231, 0xb840, v231
	v_add_u32_e32 v211, s6, v210
	s_nop 0
	s_load_dwordx8 s[4:11], s[0:1], 0x10
	v_add_u32_e32 v232, 0x24e80, v228
	ds_read_b32 v244, v232
	ds_read_b32 v245, v232 offset:128
	ds_read_b128 v[194:197], v237 offset:36928
	ds_read_b128 v[198:201], v237 offset:36944
	ds_read_b128 v[202:205], v237 offset:36960
	ds_read_b128 v[206:209], v237 offset:36976
	ds_read_b128 v[212:215], v237 offset:37056
	ds_read_b128 v[216:219], v237 offset:37072
	ds_read_b128 v[220:223], v237 offset:37088
	ds_read_b128 v[224:227], v237 offset:37104
	ds_read_b128 v[162:165], v236 offset:16384
	ds_read_b128 v[166:169], v236 offset:16416
	ds_read_b128 v[170:173], v236 offset:16448
	ds_read_b128 v[174:177], v236 offset:16480
	s_waitcnt lgkmcnt(0)
	v_mfma_f32_32x32x16_bf16 v[2:17], v[94:97], v[162:165], v[194:209]
	v_mfma_f32_32x32x16_bf16 v[18:33], v[46:49], v[162:165], v[212:227]
	v_mfma_f32_32x32x16_bf16 v[2:17], v[90:93], v[166:169], v[2:17]
	v_mfma_f32_32x32x16_bf16 v[18:33], v[42:45], v[166:169], v[18:33]
	v_mfma_f32_32x32x16_bf16 v[2:17], v[86:89], v[170:173], v[2:17]
	ds_read_b128 v[178:181], v236 offset:20992
	v_mfma_f32_32x32x16_bf16 v[18:33], v[38:41], v[170:173], v[18:33]
	ds_read_b128 v[182:185], v236 offset:21024
	v_mfma_f32_32x32x16_bf16 v[2:17], v[82:85], v[174:177], v[2:17]
	ds_read_b128 v[186:189], v236 offset:21056
	v_mfma_f32_32x32x16_bf16 v[18:33], v[34:37], v[174:177], v[18:33]
	ds_read_b128 v[190:193], v236 offset:21088
	s_waitcnt lgkmcnt(0)
	v_mfma_f32_32x32x16_bf16 v[130:145], v[94:97], v[178:181], v[194:209]
	v_mfma_f32_32x32x16_bf16 v[146:161], v[46:49], v[178:181], v[212:227]
	v_mfma_f32_32x32x16_bf16 v[130:145], v[90:93], v[182:185], v[130:145]
	v_mfma_f32_32x32x16_bf16 v[146:161], v[42:45], v[182:185], v[146:161]
	s_nop 7
	ds_write_b128 v238, v[2:5] offset:0
	ds_write_b128 v238, v[6:9] offset:16
	ds_write_b128 v238, v[10:13] offset:32
	ds_write_b128 v238, v[14:17] offset:48
	ds_write_b128 v238, v[18:21] offset:128
	ds_write_b128 v238, v[22:25] offset:144
	ds_write_b128 v238, v[26:29] offset:160
	ds_write_b128 v238, v[30:33] offset:176
	v_mfma_f32_32x32x16_bf16 v[130:145], v[86:89], v[186:189], v[130:145]
	ds_read_b128 v[162:165], v236 offset:25600
	v_mfma_f32_32x32x16_bf16 v[146:161], v[38:41], v[186:189], v[146:161]
	ds_read_b128 v[166:169], v236 offset:25632
	v_mfma_f32_32x32x16_bf16 v[130:145], v[82:85], v[190:193], v[130:145]
	ds_read_b128 v[170:173], v236 offset:25664
	v_mfma_f32_32x32x16_bf16 v[146:161], v[34:37], v[190:193], v[146:161]
	ds_read_b128 v[174:177], v236 offset:25696
	s_waitcnt lgkmcnt(0)
	v_mfma_f32_32x32x16_bf16 v[2:17], v[94:97], v[162:165], v[194:209]
	v_mfma_f32_32x32x16_bf16 v[18:33], v[46:49], v[162:165], v[212:227]
	v_mfma_f32_32x32x16_bf16 v[2:17], v[90:93], v[166:169], v[2:17]
	v_mfma_f32_32x32x16_bf16 v[18:33], v[42:45], v[166:169], v[18:33]
	s_nop 7
	v_add_u32_e32 v239, 0x8200, v238
	ds_write_b128 v239, v[130:133] offset:0
	ds_write_b128 v239, v[134:137] offset:16
	ds_write_b128 v239, v[138:141] offset:32
	ds_write_b128 v239, v[142:145] offset:48
	ds_write_b128 v239, v[146:149] offset:128
	ds_write_b128 v239, v[150:153] offset:144
	ds_write_b128 v239, v[154:157] offset:160
	ds_write_b128 v239, v[158:161] offset:176
	v_mfma_f32_32x32x16_bf16 v[2:17], v[86:89], v[170:173], v[2:17]
	ds_read_b128 v[178:181], v236 offset:30208
	v_mfma_f32_32x32x16_bf16 v[18:33], v[38:41], v[170:173], v[18:33]
	ds_read_b128 v[182:185], v236 offset:30240
	v_mfma_f32_32x32x16_bf16 v[2:17], v[82:85], v[174:177], v[2:17]
	ds_read_b128 v[186:189], v236 offset:30272
	v_mfma_f32_32x32x16_bf16 v[18:33], v[34:37], v[174:177], v[18:33]
	ds_read_b128 v[190:193], v236 offset:30304
	s_waitcnt lgkmcnt(0)
	v_mfma_f32_32x32x16_bf16 v[130:145], v[94:97], v[178:181], v[194:209]
	v_mfma_f32_32x32x16_bf16 v[146:161], v[46:49], v[178:181], v[212:227]
	v_mfma_f32_32x32x16_bf16 v[130:145], v[90:93], v[182:185], v[130:145]
	v_mfma_f32_32x32x16_bf16 v[146:161], v[42:45], v[182:185], v[146:161]
	s_nop 7
	v_add_u32_e32 v239, 0x10400, v238
	ds_write_b128 v239, v[2:5] offset:0
	ds_write_b128 v239, v[6:9] offset:16
	ds_write_b128 v239, v[10:13] offset:32
	ds_write_b128 v239, v[14:17] offset:48
	ds_write_b128 v239, v[18:21] offset:128
	ds_write_b128 v239, v[22:25] offset:144
	ds_write_b128 v239, v[26:29] offset:160
	ds_write_b128 v239, v[30:33] offset:176
	v_mfma_f32_32x32x16_bf16 v[130:145], v[86:89], v[186:189], v[130:145]
	v_mfma_f32_32x32x16_bf16 v[146:161], v[38:41], v[186:189], v[146:161]
	v_mfma_f32_32x32x16_bf16 v[130:145], v[82:85], v[190:193], v[130:145]
	v_mfma_f32_32x32x16_bf16 v[146:161], v[34:37], v[190:193], v[146:161]
	s_nop 7
	s_nop 7
	v_cmp_gt_u32_e32 vcc, 16, v228
	s_and_saveexec_b64 s[20:21], vcc
	v_add_u32_e32 v239, 0x18600, v238
	ds_write_b128 v239, v[130:133] offset:0
	ds_write_b128 v239, v[134:137] offset:16
	ds_write_b128 v239, v[138:141] offset:32
	ds_write_b128 v239, v[142:145] offset:48
	ds_write_b128 v239, v[146:149] offset:128
	ds_write_b128 v239, v[150:153] offset:144
	ds_write_b128 v239, v[154:157] offset:160
	ds_write_b128 v239, v[158:161] offset:176
	s_or_b64 exec, exec, s[20:21]
	s_mov_b32 s12, 0xbeb17218
	v_mov_b32_e32 v235, 0xc038aa3b
	v_add_u32_e32 v233, v231, v244
	v_add_u32_e32 v234, v231, v245
	ds_read_b128 v[2:5], v233 offset:0
	ds_read_b128 v[6:9], v233 offset:16
	ds_read_b128 v[10:13], v233 offset:32
	ds_read_b128 v[14:17], v233 offset:48
	ds_read_b128 v[18:21], v233 offset:128
	ds_read_b128 v[22:25], v233 offset:144
	ds_read_b128 v[26:29], v233 offset:160
	ds_read_b128 v[30:33], v233 offset:176
	ds_read_b128 v[34:37], v234 offset:0
	ds_read_b128 v[38:41], v234 offset:16
	ds_read_b128 v[42:45], v234 offset:32
	ds_read_b128 v[46:49], v234 offset:48
	v_mov_b32_e32 v194, 0
	v_mov_b32_e32 v195, 0
	v_mov_b32_e32 v196, 0
	v_mov_b32_e32 v197, 0
	v_mov_b32_e32 v198, 0
	v_mov_b32_e32 v199, 0
	v_mov_b32_e32 v200, 0
	v_mov_b32_e32 v201, 0
	v_mov_b32_e32 v202, 0
	v_mov_b32_e32 v203, 0
	v_mov_b32_e32 v204, 0
	v_mov_b32_e32 v205, 0
	v_mov_b32_e32 v206, 0
	v_mov_b32_e32 v207, 0
	v_mov_b32_e32 v208, 0
	v_mov_b32_e32 v209, 0
	v_add_u32_e32 v232, 0x100, v232
	s_movk_i32 s16, 18
	s_waitcnt vmcnt(0) lgkmcnt(0)
	ds_read_b128 v[82:85], v234 offset:128
	ds_read_b128 v[86:89], v234 offset:144
	ds_read_b128 v[90:93], v234 offset:160
	ds_read_b128 v[94:97], v234 offset:176
	ds_read2_b32 v[244:245], v232 offset1:32
	v_exp_f32_e32 v212, v4
	v_exp_f32_e32 v213, v8
	v_exp_f32_e32 v214, v12
	v_exp_f32_e32 v215, v16
	v_exp_f32_e32 v217, v2
	v_fma_f32 v251, v212, s12, s12
	v_exp_f32_e32 v218, v6
	v_fma_f32 v252, v213, s12, s12
	v_exp_f32_e32 v219, v10
	v_fma_f32 v253, v214, s12, s12
	v_exp_f32_e32 v220, v14
	v_fma_f32 v254, v215, s12, s12
	v_fmac_f32_e32 v251, v217, v251
	v_fmac_f32_e32 v252, v218, v252
	v_fmac_f32_e32 v253, v219, v253
	v_fmac_f32_e32 v254, v220, v254
	v_rcp_f32_e32 v217, v251
	v_rcp_f32_e32 v218, v252
	v_rcp_f32_e32 v219, v253
	v_rcp_f32_e32 v220, v254
	v_exp_f32_e32 v246, v5
	v_fma_f32 v194, -v212, v217, v217
	v_exp_f32_e32 v247, v9
	v_fma_f32 v195, -v213, v218, v218
	v_exp_f32_e32 v248, v13
	v_fma_f32 v196, -v214, v219, v219
	v_exp_f32_e32 v249, v17
	v_fma_f32 v197, -v215, v220, v220
	v_exp_f32_e32 v212, v194
	v_add_f32_e32 v246, 1.0, v246
	v_exp_f32_e32 v213, v195
	v_add_f32_e32 v247, 1.0, v247
	v_exp_f32_e32 v214, v196
	v_add_f32_e32 v248, 1.0, v248
	v_exp_f32_e32 v215, v197
	v_add_f32_e32 v249, 1.0, v249
	v_fmac_f32_e32 v246, v246, v212
	v_fmac_f32_e32 v247, v247, v213
	v_fmac_f32_e32 v248, v248, v214
	v_fmac_f32_e32 v249, v249, v215
	v_rcp_f32_e32 v246, v246
	v_rcp_f32_e32 v247, v247
	v_rcp_f32_e32 v248, v248
	v_rcp_f32_e32 v249, v249
	v_fma_f32 v246, -v212, v246, v246
	v_fma_f32 v247, -v213, v247, v247
	v_fma_f32 v248, -v214, v248, v248
	v_fma_f32 v249, -v215, v249, v249
	v_cvt_pk_bf16_f32 v236, v246, v247
	v_cvt_pk_bf16_f32 v237, v248, v249
	s_waitcnt lgkmcnt(0)
	v_add_u32_e32 v233, v231, v244
	ds_read_b128 v[2:5], v233 offset:0
	ds_read_b128 v[6:9], v233 offset:16
	ds_read_b128 v[10:13], v233 offset:32
	ds_read_b128 v[14:17], v233 offset:48
	v_exp_f32_e32 v212, v20
	v_exp_f32_e32 v213, v24
	v_exp_f32_e32 v214, v28
	v_exp_f32_e32 v215, v32
	v_exp_f32_e32 v217, v18
	v_fma_f32 v251, v212, s12, s12
	v_exp_f32_e32 v218, v22
	v_fma_f32 v252, v213, s12, s12
	v_exp_f32_e32 v219, v26
	v_fma_f32 v253, v214, s12, s12
	v_exp_f32_e32 v220, v30
	v_fma_f32 v254, v215, s12, s12
	v_fmac_f32_e32 v251, v217, v251
	v_fmac_f32_e32 v252, v218, v252
	v_fmac_f32_e32 v253, v219, v253
	v_fmac_f32_e32 v254, v220, v254
	v_rcp_f32_e32 v217, v251
	v_rcp_f32_e32 v218, v252
	v_rcp_f32_e32 v219, v253
	v_rcp_f32_e32 v220, v254
	v_exp_f32_e32 v246, v21
	v_fma_f32 v198, -v212, v217, v217
	v_exp_f32_e32 v247, v25
	v_fma_f32 v199, -v213, v218, v218
	v_exp_f32_e32 v248, v29
	v_fma_f32 v200, -v214, v219, v219
	v_exp_f32_e32 v249, v33
	v_fma_f32 v201, -v215, v220, v220
	v_exp_f32_e32 v212, v198
	v_add_f32_e32 v246, 1.0, v246
	v_exp_f32_e32 v213, v199
	v_add_f32_e32 v247, 1.0, v247
	v_exp_f32_e32 v214, v200
	v_add_f32_e32 v248, 1.0, v248
	v_exp_f32_e32 v215, v201
	v_add_f32_e32 v249, 1.0, v249
	v_fmac_f32_e32 v246, v246, v212
	v_fmac_f32_e32 v247, v247, v213
	v_fmac_f32_e32 v248, v248, v214
	v_fmac_f32_e32 v249, v249, v215
	v_rcp_f32_e32 v246, v246
	v_rcp_f32_e32 v247, v247
	v_rcp_f32_e32 v248, v248
	v_rcp_f32_e32 v249, v249
	v_fma_f32 v246, -v212, v246, v246
	v_fma_f32 v247, -v213, v247, v247
	v_fma_f32 v248, -v214, v248, v248
	v_fma_f32 v249, -v215, v249, v249
	v_cvt_pk_bf16_f32 v238, v246, v247
	v_cvt_pk_bf16_f32 v239, v248, v249
	ds_write_b128 v211, v[236:239] offset:0
	ds_read_b128 v[18:21], v233 offset:128
	ds_read_b128 v[22:25], v233 offset:144
	ds_read_b128 v[26:29], v233 offset:160
	ds_read_b128 v[30:33], v233 offset:176
	v_exp_f32_e32 v212, v36
	v_exp_f32_e32 v213, v40
	v_exp_f32_e32 v214, v44
	v_exp_f32_e32 v215, v48
	v_exp_f32_e32 v217, v34
	v_fma_f32 v251, v212, s12, s12
	v_exp_f32_e32 v218, v38
	v_fma_f32 v252, v213, s12, s12
	v_exp_f32_e32 v219, v42
	v_fma_f32 v253, v214, s12, s12
	v_exp_f32_e32 v220, v46
	v_fma_f32 v254, v215, s12, s12
	s_waitcnt lgkmcnt(4)
	s_barrier
	ds_read_b128 v[130:133], v210 offset:0
	ds_read_b128 v[134:137], v210 offset:1024
	v_fmac_f32_e32 v251, v217, v251
	v_fmac_f32_e32 v252, v218, v252
	v_fmac_f32_e32 v253, v219, v253
	v_fmac_f32_e32 v254, v220, v254
	ds_read_b128 v[138:141], v210 offset:2048
	ds_read_b128 v[142:145], v210 offset:3072
	v_rcp_f32_e32 v217, v251
	v_rcp_f32_e32 v218, v252
	v_rcp_f32_e32 v219, v253
	v_rcp_f32_e32 v220, v254
	ds_read_b128 v[146:149], v210 offset:4096
	ds_read_b128 v[150:153], v210 offset:5120
	v_exp_f32_e32 v246, v37
	v_fma_f32 v202, -v212, v217, v217
	v_exp_f32_e32 v247, v41
	v_fma_f32 v203, -v213, v218, v218
	v_exp_f32_e32 v248, v45
	v_fma_f32 v204, -v214, v219, v219
	v_exp_f32_e32 v249, v49
	v_fma_f32 v205, -v215, v220, v220
	ds_read_b128 v[154:157], v210 offset:6144
	ds_read_b128 v[158:161], v210 offset:7168
	v_exp_f32_e32 v212, v202
	v_add_f32_e32 v246, 1.0, v246
	v_exp_f32_e32 v213, v203
	v_add_f32_e32 v247, 1.0, v247
	v_exp_f32_e32 v214, v204
	v_add_f32_e32 v248, 1.0, v248
	v_exp_f32_e32 v215, v205
	v_add_f32_e32 v249, 1.0, v249
	v_fmac_f32_e32 v246, v246, v212
	v_fmac_f32_e32 v247, v247, v213
	v_fmac_f32_e32 v248, v248, v214
	v_fmac_f32_e32 v249, v249, v215
	v_rcp_f32_e32 v246, v246
	v_rcp_f32_e32 v247, v247
	v_rcp_f32_e32 v248, v248
	v_rcp_f32_e32 v249, v249
	v_fma_f32 v246, -v212, v246, v246
	v_fma_f32 v247, -v213, v247, v247
	v_fma_f32 v248, -v214, v248, v248
	v_fma_f32 v249, -v215, v249, v249
	v_cvt_pk_bf16_f32 v236, v246, v247
	v_cvt_pk_bf16_f32 v237, v248, v249
	s_waitcnt lgkmcnt(0)
	v_mfma_f32_32x32x16_bf16 v[2:17], v[126:129], v[130:133], v[2:17]
	v_add_u32_e32 v234, v231, v245
	ds_read_b128 v[34:37], v234 offset:0
	ds_read_b128 v[38:41], v234 offset:16
	ds_read_b128 v[42:45], v234 offset:32
	ds_read_b128 v[46:49], v234 offset:48
	v_add_u32_e32 v232, 0x100, v232
	v_exp_f32_e32 v212, v84
	v_exp_f32_e32 v213, v88
	v_exp_f32_e32 v214, v92
	v_exp_f32_e32 v215, v96
	v_mfma_f32_32x32x16_bf16 v[2:17], v[122:125], v[134:137], v[2:17]
	v_exp_f32_e32 v217, v82
	v_fma_f32 v251, v212, s12, s12
	v_exp_f32_e32 v218, v86
	v_fma_f32 v252, v213, s12, s12
	v_exp_f32_e32 v219, v90
	v_fma_f32 v253, v214, s12, s12
	v_exp_f32_e32 v220, v94
	v_fma_f32 v254, v215, s12, s12
	v_mfma_f32_32x32x16_bf16 v[2:17], v[118:121], v[138:141], v[2:17]
	v_fmac_f32_e32 v251, v217, v251
	v_fmac_f32_e32 v252, v218, v252
	v_fmac_f32_e32 v253, v219, v253
	v_fmac_f32_e32 v254, v220, v254
	v_mfma_f32_32x32x16_bf16 v[2:17], v[114:117], v[142:145], v[2:17]
	v_rcp_f32_e32 v217, v251
	v_rcp_f32_e32 v218, v252
	v_rcp_f32_e32 v219, v253
	v_rcp_f32_e32 v220, v254
	v_mfma_f32_32x32x16_bf16 v[2:17], v[110:113], v[146:149], v[2:17]
	v_exp_f32_e32 v246, v85
	v_fma_f32 v206, -v212, v217, v217
	v_exp_f32_e32 v247, v89
	v_fma_f32 v207, -v213, v218, v218
	v_exp_f32_e32 v248, v93
	v_fma_f32 v208, -v214, v219, v219
	v_exp_f32_e32 v249, v97
	v_fma_f32 v209, -v215, v220, v220
	v_mfma_f32_32x32x16_bf16 v[2:17], v[106:109], v[150:153], v[2:17]
	v_mfma_f32_32x32x16_bf16 v[2:17], v[102:105], v[154:157], v[2:17]
	v_exp_f32_e32 v212, v206
	v_add_f32_e32 v246, 1.0, v246
	v_exp_f32_e32 v213, v207
	v_add_f32_e32 v247, 1.0, v247
	v_exp_f32_e32 v214, v208
	v_add_f32_e32 v248, 1.0, v248
	v_exp_f32_e32 v215, v209
	v_add_f32_e32 v249, 1.0, v249
	v_fmac_f32_e32 v246, v246, v212
	v_fmac_f32_e32 v247, v247, v213
	v_fmac_f32_e32 v248, v248, v214
	v_fmac_f32_e32 v249, v249, v215
	v_mfma_f32_32x32x16_bf16 v[2:17], v[98:101], v[158:161], v[2:17]
	v_rcp_f32_e32 v246, v246
	v_rcp_f32_e32 v247, v247
	v_rcp_f32_e32 v248, v248
	v_rcp_f32_e32 v249, v249
	v_fma_f32 v246, -v212, v246, v246
	v_fma_f32 v247, -v213, v247, v247
	v_fma_f32 v248, -v214, v248, v248
	v_fma_f32 v249, -v215, v249, v249
	v_cvt_pk_bf16_f32 v238, v246, v247
	v_cvt_pk_bf16_f32 v239, v248, v249
	ds_write_b128 v211, v[236:239] offset:8192
	.p2align 6
.Llight_loop:
	v_mfma_f32_32x32x16_bf16 v[18:33], v[78:81], v[130:133], v[18:33]
	ds_read_b128 v[82:85], v234 offset:128
	ds_read_b128 v[86:89], v234 offset:144
	ds_read_b128 v[90:93], v234 offset:160
	ds_read_b128 v[94:97], v234 offset:176
	ds_read2_b32 v[244:245], v232 offset1:32
	v_exp_f32_e32 v212, v4
	v_exp_f32_e32 v213, v8
	v_exp_f32_e32 v214, v12
	v_exp_f32_e32 v215, v16
	v_mfma_f32_32x32x16_bf16 v[18:33], v[74:77], v[134:137], v[18:33]
	v_exp_f32_e32 v217, v2
	v_fma_f32 v251, v212, s12, s12
	v_exp_f32_e32 v218, v6
	v_fma_f32 v252, v213, s12, s12
	v_exp_f32_e32 v219, v10
	v_fma_f32 v253, v214, s12, s12
	v_exp_f32_e32 v220, v14
	v_fma_f32 v254, v215, s12, s12
	s_waitcnt lgkmcnt(5)
	s_barrier
	v_mfma_f32_32x32x16_bf16 v[18:33], v[70:73], v[138:141], v[18:33]
	ds_read_b128 v[162:165], v210 offset:8192
	ds_read_b128 v[166:169], v210 offset:9216
	v_exp_f32_e32 v221, v3
	v_fmac_f32_e32 v251, v217, v251
	v_exp_f32_e32 v222, v7
	v_fmac_f32_e32 v252, v218, v252
	v_exp_f32_e32 v223, v11
	v_fmac_f32_e32 v253, v219, v253
	v_exp_f32_e32 v224, v15
	v_fmac_f32_e32 v254, v220, v254
	v_mfma_f32_32x32x16_bf16 v[18:33], v[66:69], v[142:145], v[18:33]
	ds_read_b128 v[170:173], v210 offset:10240
	ds_read_b128 v[174:177], v210 offset:11264
	v_rcp_f32_e32 v217, v251
	v_add_f32_e32 v221, 1.0, v221
	v_rcp_f32_e32 v218, v252
	v_add_f32_e32 v222, 1.0, v222
	v_rcp_f32_e32 v219, v253
	v_add_f32_e32 v223, 1.0, v223
	v_rcp_f32_e32 v220, v254
	v_add_f32_e32 v224, 1.0, v224
	v_mfma_f32_32x32x16_bf16 v[18:33], v[62:65], v[146:149], v[18:33]
	ds_read_b128 v[178:181], v210 offset:12288
	ds_read_b128 v[182:185], v210 offset:13312
	v_rcp_f32_e32 v221, v221
	v_fma_f32 v240, -v212, v217, v217
	v_rcp_f32_e32 v222, v222
	v_fma_f32 v241, -v213, v218, v218
	v_rcp_f32_e32 v223, v223
	v_fma_f32 v242, -v214, v219, v219
	v_rcp_f32_e32 v224, v224
	v_fma_f32 v243, -v215, v220, v220
	v_mfma_f32_32x32x16_bf16 v[18:33], v[58:61], v[150:153], v[18:33]
	ds_read_b128 v[186:189], v210 offset:14336
	ds_read_b128 v[190:193], v210 offset:15360
	v_exp_f32_e32 v246, v5
	v_fma_f32 v194, v221, v194, v240
	v_exp_f32_e32 v247, v9
	v_fma_f32 v195, v222, v195, v241
	v_exp_f32_e32 v248, v13
	v_fma_f32 v196, v223, v196, v242
	v_exp_f32_e32 v249, v17
	v_fma_f32 v197, v224, v197, v243
	v_mfma_f32_32x32x16_bf16 v[18:33], v[54:57], v[154:157], v[18:33]
	v_exp_f32_e32 v212, v194
	v_add_f32_e32 v246, 1.0, v246
	v_exp_f32_e32 v213, v195
	v_add_f32_e32 v247, 1.0, v247
	v_exp_f32_e32 v214, v196
	v_add_f32_e32 v248, 1.0, v248
	v_exp_f32_e32 v215, v197
	v_add_f32_e32 v249, 1.0, v249
	v_fmac_f32_e32 v246, v246, v212
	v_fmac_f32_e32 v247, v247, v213
	v_fmac_f32_e32 v248, v248, v214
	v_fmac_f32_e32 v249, v249, v215
	v_mfma_f32_32x32x16_bf16 v[18:33], v[50:53], v[158:161], v[18:33]
	v_rcp_f32_e32 v246, v246
	v_rcp_f32_e32 v247, v247
	v_rcp_f32_e32 v248, v248
	v_rcp_f32_e32 v249, v249
	v_fma_f32 v246, -v212, v246, v246
	v_fma_f32 v247, -v213, v247, v247
	v_fma_f32 v248, -v214, v248, v248
	v_fma_f32 v249, -v215, v249, v249
	v_cvt_pk_bf16_f32 v236, v246, v247
	v_cvt_pk_bf16_f32 v237, v248, v249
	s_waitcnt lgkmcnt(0)
	v_mfma_f32_32x32x16_bf16 v[34:49], v[126:129], v[162:165], v[34:49]
	v_add_u32_e32 v233, v231, v244
	ds_read_b128 v[2:5], v233 offset:0
	ds_read_b128 v[6:9], v233 offset:16
	ds_read_b128 v[10:13], v233 offset:32
	ds_read_b128 v[14:17], v233 offset:48
	v_exp_f32_e32 v212, v20
	v_exp_f32_e32 v213, v24
	v_exp_f32_e32 v214, v28
	v_exp_f32_e32 v215, v32
	v_mfma_f32_32x32x16_bf16 v[34:49], v[122:125], v[166:169], v[34:49]
	v_exp_f32_e32 v217, v18
	v_fma_f32 v251, v212, s12, s12
	v_exp_f32_e32 v218, v22
	v_fma_f32 v252, v213, s12, s12
	v_exp_f32_e32 v219, v26
	v_fma_f32 v253, v214, s12, s12
	v_exp_f32_e32 v220, v30
	v_fma_f32 v254, v215, s12, s12
	v_mfma_f32_32x32x16_bf16 v[34:49], v[118:121], v[170:173], v[34:49]
	v_exp_f32_e32 v221, v19
	v_fmac_f32_e32 v251, v217, v251
	v_exp_f32_e32 v222, v23
	v_fmac_f32_e32 v252, v218, v252
	v_exp_f32_e32 v223, v27
	v_fmac_f32_e32 v253, v219, v253
	v_exp_f32_e32 v224, v31
	v_fmac_f32_e32 v254, v220, v254
	v_mfma_f32_32x32x16_bf16 v[34:49], v[114:117], v[174:177], v[34:49]
	v_rcp_f32_e32 v217, v251
	v_add_f32_e32 v221, 1.0, v221
	v_rcp_f32_e32 v218, v252
	v_add_f32_e32 v222, 1.0, v222
	v_rcp_f32_e32 v219, v253
	v_add_f32_e32 v223, 1.0, v223
	v_rcp_f32_e32 v220, v254
	v_add_f32_e32 v224, 1.0, v224
	v_mfma_f32_32x32x16_bf16 v[34:49], v[110:113], v[178:181], v[34:49]
	v_rcp_f32_e32 v221, v221
	v_fma_f32 v240, -v212, v217, v217
	v_rcp_f32_e32 v222, v222
	v_fma_f32 v241, -v213, v218, v218
	v_rcp_f32_e32 v223, v223
	v_fma_f32 v242, -v214, v219, v219
	v_rcp_f32_e32 v224, v224
	v_fma_f32 v243, -v215, v220, v220
	v_mfma_f32_32x32x16_bf16 v[34:49], v[106:109], v[182:185], v[34:49]
	v_exp_f32_e32 v246, v21
	v_fma_f32 v198, v221, v198, v240
	v_exp_f32_e32 v247, v25
	v_fma_f32 v199, v222, v199, v241
	v_exp_f32_e32 v248, v29
	v_fma_f32 v200, v223, v200, v242
	v_exp_f32_e32 v249, v33
	v_fma_f32 v201, v224, v201, v243
	v_mfma_f32_32x32x16_bf16 v[34:49], v[102:105], v[186:189], v[34:49]
	v_exp_f32_e32 v212, v198
	v_add_f32_e32 v246, 1.0, v246
	v_exp_f32_e32 v213, v199
	v_add_f32_e32 v247, 1.0, v247
	v_exp_f32_e32 v214, v200
	v_add_f32_e32 v248, 1.0, v248
	v_exp_f32_e32 v215, v201
	v_add_f32_e32 v249, 1.0, v249
	v_fmac_f32_e32 v246, v246, v212
	v_fmac_f32_e32 v247, v247, v213
	v_fmac_f32_e32 v248, v248, v214
	v_fmac_f32_e32 v249, v249, v215
	v_mfma_f32_32x32x16_bf16 v[34:49], v[98:101], v[190:193], v[34:49]
	v_rcp_f32_e32 v246, v246
	v_rcp_f32_e32 v247, v247
	v_rcp_f32_e32 v248, v248
	v_rcp_f32_e32 v249, v249
	v_fma_f32 v246, -v212, v246, v246
	v_fma_f32 v247, -v213, v247, v247
	v_fma_f32 v248, -v214, v248, v248
	v_fma_f32 v249, -v215, v249, v249
	v_cvt_pk_bf16_f32 v238, v246, v247
	v_cvt_pk_bf16_f32 v239, v248, v249
	ds_write_b128 v211, v[236:239] offset:0
	v_mfma_f32_32x32x16_bf16 v[82:97], v[78:81], v[162:165], v[82:97]
	ds_read_b128 v[18:21], v233 offset:128
	ds_read_b128 v[22:25], v233 offset:144
	ds_read_b128 v[26:29], v233 offset:160
	ds_read_b128 v[30:33], v233 offset:176
	v_exp_f32_e32 v212, v36
	v_exp_f32_e32 v213, v40
	v_exp_f32_e32 v214, v44
	v_exp_f32_e32 v215, v48
	v_mfma_f32_32x32x16_bf16 v[82:97], v[74:77], v[166:169], v[82:97]
	v_exp_f32_e32 v217, v34
	v_fma_f32 v251, v212, s12, s12
	v_exp_f32_e32 v218, v38
	v_fma_f32 v252, v213, s12, s12
	v_exp_f32_e32 v219, v42
	v_fma_f32 v253, v214, s12, s12
	v_exp_f32_e32 v220, v46
	v_fma_f32 v254, v215, s12, s12
	s_waitcnt lgkmcnt(4)
	s_barrier
	v_mfma_f32_32x32x16_bf16 v[82:97], v[70:73], v[170:173], v[82:97]
	ds_read_b128 v[130:133], v210 offset:0
	ds_read_b128 v[134:137], v210 offset:1024
	v_exp_f32_e32 v221, v35
	v_fmac_f32_e32 v251, v217, v251
	v_exp_f32_e32 v222, v39
	v_fmac_f32_e32 v252, v218, v252
	v_exp_f32_e32 v223, v43
	v_fmac_f32_e32 v253, v219, v253
	v_exp_f32_e32 v224, v47
	v_fmac_f32_e32 v254, v220, v254
	v_mfma_f32_32x32x16_bf16 v[82:97], v[66:69], v[174:177], v[82:97]
	ds_read_b128 v[138:141], v210 offset:2048
	ds_read_b128 v[142:145], v210 offset:3072
	v_rcp_f32_e32 v217, v251
	v_add_f32_e32 v221, 1.0, v221
	v_rcp_f32_e32 v218, v252
	v_add_f32_e32 v222, 1.0, v222
	v_rcp_f32_e32 v219, v253
	v_add_f32_e32 v223, 1.0, v223
	v_rcp_f32_e32 v220, v254
	v_add_f32_e32 v224, 1.0, v224
	v_mfma_f32_32x32x16_bf16 v[82:97], v[62:65], v[178:181], v[82:97]
	ds_read_b128 v[146:149], v210 offset:4096
	ds_read_b128 v[150:153], v210 offset:5120
	v_rcp_f32_e32 v221, v221
	v_fma_f32 v240, -v212, v217, v217
	v_rcp_f32_e32 v222, v222
	v_fma_f32 v241, -v213, v218, v218
	v_rcp_f32_e32 v223, v223
	v_fma_f32 v242, -v214, v219, v219
	v_rcp_f32_e32 v224, v224
	v_fma_f32 v243, -v215, v220, v220
	v_mfma_f32_32x32x16_bf16 v[82:97], v[58:61], v[182:185], v[82:97]
	ds_read_b128 v[154:157], v210 offset:6144
	ds_read_b128 v[158:161], v210 offset:7168
	v_exp_f32_e32 v246, v37
	v_fma_f32 v202, v221, v202, v240
	v_exp_f32_e32 v247, v41
	v_fma_f32 v203, v222, v203, v241
	v_exp_f32_e32 v248, v45
	v_fma_f32 v204, v223, v204, v242
	v_exp_f32_e32 v249, v49
	v_fma_f32 v205, v224, v205, v243
	v_mfma_f32_32x32x16_bf16 v[82:97], v[54:57], v[186:189], v[82:97]
	v_exp_f32_e32 v212, v202
	v_add_f32_e32 v246, 1.0, v246
	v_exp_f32_e32 v213, v203
	v_add_f32_e32 v247, 1.0, v247
	v_exp_f32_e32 v214, v204
	v_add_f32_e32 v248, 1.0, v248
	v_exp_f32_e32 v215, v205
	v_add_f32_e32 v249, 1.0, v249
	v_fmac_f32_e32 v246, v246, v212
	v_fmac_f32_e32 v247, v247, v213
	v_fmac_f32_e32 v248, v248, v214
	v_fmac_f32_e32 v249, v249, v215
	v_mfma_f32_32x32x16_bf16 v[82:97], v[50:53], v[190:193], v[82:97]
	v_rcp_f32_e32 v246, v246
	v_rcp_f32_e32 v247, v247
	v_rcp_f32_e32 v248, v248
	v_rcp_f32_e32 v249, v249
	v_fma_f32 v246, -v212, v246, v246
	v_fma_f32 v247, -v213, v247, v247
	v_fma_f32 v248, -v214, v248, v248
	v_fma_f32 v249, -v215, v249, v249
	v_cvt_pk_bf16_f32 v236, v246, v247
	v_cvt_pk_bf16_f32 v237, v248, v249
	s_waitcnt lgkmcnt(0)
	v_mfma_f32_32x32x16_bf16 v[2:17], v[126:129], v[130:133], v[2:17]
	v_add_u32_e32 v234, v231, v245
	ds_read_b128 v[34:37], v234 offset:0
	ds_read_b128 v[38:41], v234 offset:16
	ds_read_b128 v[42:45], v234 offset:32
	ds_read_b128 v[46:49], v234 offset:48
	v_add_u32_e32 v232, 0x100, v232
	v_exp_f32_e32 v212, v84
	v_exp_f32_e32 v213, v88
	v_exp_f32_e32 v214, v92
	v_exp_f32_e32 v215, v96
	v_mfma_f32_32x32x16_bf16 v[2:17], v[122:125], v[134:137], v[2:17]
	v_exp_f32_e32 v217, v82
	v_fma_f32 v251, v212, s12, s12
	v_exp_f32_e32 v218, v86
	v_fma_f32 v252, v213, s12, s12
	v_exp_f32_e32 v219, v90
	v_fma_f32 v253, v214, s12, s12
	v_exp_f32_e32 v220, v94
	v_fma_f32 v254, v215, s12, s12
	v_mfma_f32_32x32x16_bf16 v[2:17], v[118:121], v[138:141], v[2:17]
	v_exp_f32_e32 v221, v83
	v_fmac_f32_e32 v251, v217, v251
	v_exp_f32_e32 v222, v87
	v_fmac_f32_e32 v252, v218, v252
	v_exp_f32_e32 v223, v91
	v_fmac_f32_e32 v253, v219, v253
	v_exp_f32_e32 v224, v95
	v_fmac_f32_e32 v254, v220, v254
	v_mfma_f32_32x32x16_bf16 v[2:17], v[114:117], v[142:145], v[2:17]
	v_rcp_f32_e32 v217, v251
	v_add_f32_e32 v221, 1.0, v221
	v_rcp_f32_e32 v218, v252
	v_add_f32_e32 v222, 1.0, v222
	v_rcp_f32_e32 v219, v253
	v_add_f32_e32 v223, 1.0, v223
	v_rcp_f32_e32 v220, v254
	v_add_f32_e32 v224, 1.0, v224
	v_mfma_f32_32x32x16_bf16 v[2:17], v[110:113], v[146:149], v[2:17]
	v_rcp_f32_e32 v221, v221
	v_fma_f32 v240, -v212, v217, v217
	v_rcp_f32_e32 v222, v222
	v_fma_f32 v241, -v213, v218, v218
	v_rcp_f32_e32 v223, v223
	v_fma_f32 v242, -v214, v219, v219
	v_rcp_f32_e32 v224, v224
	v_fma_f32 v243, -v215, v220, v220
	v_mfma_f32_32x32x16_bf16 v[2:17], v[106:109], v[150:153], v[2:17]
	v_exp_f32_e32 v246, v85
	v_fma_f32 v206, v221, v206, v240
	v_exp_f32_e32 v247, v89
	v_fma_f32 v207, v222, v207, v241
	v_exp_f32_e32 v248, v93
	v_fma_f32 v208, v223, v208, v242
	v_exp_f32_e32 v249, v97
	v_fma_f32 v209, v224, v209, v243
	v_mfma_f32_32x32x16_bf16 v[2:17], v[102:105], v[154:157], v[2:17]
	v_exp_f32_e32 v212, v206
	v_add_f32_e32 v246, 1.0, v246
	v_exp_f32_e32 v213, v207
	v_add_f32_e32 v247, 1.0, v247
	v_exp_f32_e32 v214, v208
	v_add_f32_e32 v248, 1.0, v248
	v_exp_f32_e32 v215, v209
	v_add_f32_e32 v249, 1.0, v249
	v_fmac_f32_e32 v246, v246, v212
	v_fmac_f32_e32 v247, v247, v213
	v_fmac_f32_e32 v248, v248, v214
	v_fmac_f32_e32 v249, v249, v215
	v_mfma_f32_32x32x16_bf16 v[2:17], v[98:101], v[158:161], v[2:17]
	v_rcp_f32_e32 v246, v246
	v_rcp_f32_e32 v247, v247
	v_rcp_f32_e32 v248, v248
	v_rcp_f32_e32 v249, v249
	v_fma_f32 v246, -v212, v246, v246
	v_fma_f32 v247, -v213, v247, v247
	v_fma_f32 v248, -v214, v248, v248
	v_fma_f32 v249, -v215, v249, v249
	v_cvt_pk_bf16_f32 v238, v246, v247
	v_cvt_pk_bf16_f32 v239, v248, v249
	ds_write_b128 v211, v[236:239] offset:8192
	s_sub_u32 s16, s16, 1
	s_cmp_lg_u32 s16, 0
	s_cbranch_scc1 .Llight_loop
	v_mfma_f32_32x32x16_bf16 v[18:33], v[78:81], v[130:133], v[18:33]
	ds_read_b128 v[82:85], v234 offset:128
	ds_read_b128 v[86:89], v234 offset:144
	ds_read_b128 v[90:93], v234 offset:160
	ds_read_b128 v[94:97], v234 offset:176
	v_exp_f32_e32 v212, v4
	v_exp_f32_e32 v213, v8
	v_exp_f32_e32 v214, v12
	v_exp_f32_e32 v215, v16
	v_mfma_f32_32x32x16_bf16 v[18:33], v[74:77], v[134:137], v[18:33]
	v_exp_f32_e32 v217, v2
	v_fma_f32 v251, v212, s12, s12
	v_exp_f32_e32 v218, v6
	v_fma_f32 v252, v213, s12, s12
	v_exp_f32_e32 v219, v10
	v_fma_f32 v253, v214, s12, s12
	v_exp_f32_e32 v220, v14
	v_fma_f32 v254, v215, s12, s12
	s_waitcnt lgkmcnt(4)
	s_barrier
	v_mfma_f32_32x32x16_bf16 v[18:33], v[70:73], v[138:141], v[18:33]
	ds_read_b128 v[162:165], v210 offset:8192
	ds_read_b128 v[166:169], v210 offset:9216
	v_exp_f32_e32 v221, v3
	v_fmac_f32_e32 v251, v217, v251
	v_exp_f32_e32 v222, v7
	v_fmac_f32_e32 v252, v218, v252
	v_exp_f32_e32 v223, v11
	v_fmac_f32_e32 v253, v219, v253
	v_exp_f32_e32 v224, v15
	v_fmac_f32_e32 v254, v220, v254
	v_mfma_f32_32x32x16_bf16 v[18:33], v[66:69], v[142:145], v[18:33]
	ds_read_b128 v[170:173], v210 offset:10240
	ds_read_b128 v[174:177], v210 offset:11264
	v_rcp_f32_e32 v217, v251
	v_add_f32_e32 v221, 1.0, v221
	v_rcp_f32_e32 v218, v252
	v_add_f32_e32 v222, 1.0, v222
	v_rcp_f32_e32 v219, v253
	v_add_f32_e32 v223, 1.0, v223
	v_rcp_f32_e32 v220, v254
	v_add_f32_e32 v224, 1.0, v224
	v_mfma_f32_32x32x16_bf16 v[18:33], v[62:65], v[146:149], v[18:33]
	ds_read_b128 v[178:181], v210 offset:12288
	ds_read_b128 v[182:185], v210 offset:13312
	v_rcp_f32_e32 v221, v221
	v_fma_f32 v240, -v212, v217, v217
	v_rcp_f32_e32 v222, v222
	v_fma_f32 v241, -v213, v218, v218
	v_rcp_f32_e32 v223, v223
	v_fma_f32 v242, -v214, v219, v219
	v_rcp_f32_e32 v224, v224
	v_fma_f32 v243, -v215, v220, v220
	v_mfma_f32_32x32x16_bf16 v[18:33], v[58:61], v[150:153], v[18:33]
	ds_read_b128 v[186:189], v210 offset:14336
	ds_read_b128 v[190:193], v210 offset:15360
	v_exp_f32_e32 v246, v5
	v_fma_f32 v194, v221, v194, v240
	v_exp_f32_e32 v247, v9
	v_fma_f32 v195, v222, v195, v241
	v_exp_f32_e32 v248, v13
	v_fma_f32 v196, v223, v196, v242
	v_exp_f32_e32 v249, v17
	v_fma_f32 v197, v224, v197, v243
	v_mfma_f32_32x32x16_bf16 v[18:33], v[54:57], v[154:157], v[18:33]
	v_exp_f32_e32 v212, v194
	v_add_f32_e32 v246, 1.0, v246
	v_exp_f32_e32 v213, v195
	v_add_f32_e32 v247, 1.0, v247
	v_exp_f32_e32 v214, v196
	v_add_f32_e32 v248, 1.0, v248
	v_exp_f32_e32 v215, v197
	v_add_f32_e32 v249, 1.0, v249
	v_fmac_f32_e32 v246, v246, v212
	v_fmac_f32_e32 v247, v247, v213
	v_fmac_f32_e32 v248, v248, v214
	v_fmac_f32_e32 v249, v249, v215
	v_mfma_f32_32x32x16_bf16 v[18:33], v[50:53], v[158:161], v[18:33]
	v_rcp_f32_e32 v246, v246
	v_rcp_f32_e32 v247, v247
	v_rcp_f32_e32 v248, v248
	v_rcp_f32_e32 v249, v249
	v_fma_f32 v246, -v212, v246, v246
	v_fma_f32 v247, -v213, v247, v247
	v_fma_f32 v248, -v214, v248, v248
	v_fma_f32 v249, -v215, v249, v249
	v_cvt_pk_bf16_f32 v236, v246, v247
	v_cvt_pk_bf16_f32 v237, v248, v249
	s_waitcnt lgkmcnt(0)
	v_mfma_f32_32x32x16_bf16 v[34:49], v[126:129], v[162:165], v[34:49]
	v_exp_f32_e32 v212, v20
	v_exp_f32_e32 v213, v24
	v_exp_f32_e32 v214, v28
	v_exp_f32_e32 v215, v32
	v_mfma_f32_32x32x16_bf16 v[34:49], v[122:125], v[166:169], v[34:49]
	v_exp_f32_e32 v217, v18
	v_fma_f32 v251, v212, s12, s12
	v_exp_f32_e32 v218, v22
	v_fma_f32 v252, v213, s12, s12
	v_exp_f32_e32 v219, v26
	v_fma_f32 v253, v214, s12, s12
	v_exp_f32_e32 v220, v30
	v_fma_f32 v254, v215, s12, s12
	v_mfma_f32_32x32x16_bf16 v[34:49], v[118:121], v[170:173], v[34:49]
	v_exp_f32_e32 v221, v19
	v_fmac_f32_e32 v251, v217, v251
	v_exp_f32_e32 v222, v23
	v_fmac_f32_e32 v252, v218, v252
	v_exp_f32_e32 v223, v27
	v_fmac_f32_e32 v253, v219, v253
	v_exp_f32_e32 v224, v31
	v_fmac_f32_e32 v254, v220, v254
	v_mfma_f32_32x32x16_bf16 v[34:49], v[114:117], v[174:177], v[34:49]
	v_rcp_f32_e32 v217, v251
	v_add_f32_e32 v221, 1.0, v221
	v_rcp_f32_e32 v218, v252
	v_add_f32_e32 v222, 1.0, v222
	v_rcp_f32_e32 v219, v253
	v_add_f32_e32 v223, 1.0, v223
	v_rcp_f32_e32 v220, v254
	v_add_f32_e32 v224, 1.0, v224
	v_mfma_f32_32x32x16_bf16 v[34:49], v[110:113], v[178:181], v[34:49]
	v_rcp_f32_e32 v221, v221
	v_fma_f32 v240, -v212, v217, v217
	v_rcp_f32_e32 v222, v222
	v_fma_f32 v241, -v213, v218, v218
	v_rcp_f32_e32 v223, v223
	v_fma_f32 v242, -v214, v219, v219
	v_rcp_f32_e32 v224, v224
	v_fma_f32 v243, -v215, v220, v220
	v_mfma_f32_32x32x16_bf16 v[34:49], v[106:109], v[182:185], v[34:49]
	v_exp_f32_e32 v246, v21
	v_fma_f32 v198, v221, v198, v240
	v_exp_f32_e32 v247, v25
	v_fma_f32 v199, v222, v199, v241
	v_exp_f32_e32 v248, v29
	v_fma_f32 v200, v223, v200, v242
	v_exp_f32_e32 v249, v33
	v_fma_f32 v201, v224, v201, v243
	v_mfma_f32_32x32x16_bf16 v[34:49], v[102:105], v[186:189], v[34:49]
	v_exp_f32_e32 v212, v198
	v_add_f32_e32 v246, 1.0, v246
	v_exp_f32_e32 v213, v199
	v_add_f32_e32 v247, 1.0, v247
	v_exp_f32_e32 v214, v200
	v_add_f32_e32 v248, 1.0, v248
	v_exp_f32_e32 v215, v201
	v_add_f32_e32 v249, 1.0, v249
	v_fmac_f32_e32 v246, v246, v212
	v_fmac_f32_e32 v247, v247, v213
	v_fmac_f32_e32 v248, v248, v214
	v_fmac_f32_e32 v249, v249, v215
	v_mfma_f32_32x32x16_bf16 v[34:49], v[98:101], v[190:193], v[34:49]
	v_rcp_f32_e32 v246, v246
	v_rcp_f32_e32 v247, v247
	v_rcp_f32_e32 v248, v248
	v_rcp_f32_e32 v249, v249
	v_fma_f32 v246, -v212, v246, v246
	v_fma_f32 v247, -v213, v247, v247
	v_fma_f32 v248, -v214, v248, v248
	v_fma_f32 v249, -v215, v249, v249
	v_cvt_pk_bf16_f32 v238, v246, v247
	v_cvt_pk_bf16_f32 v239, v248, v249
	ds_write_b128 v211, v[236:239] offset:0
	s_waitcnt lgkmcnt(0)
	s_barrier
	s_bfe_u32 s20, s19, 0x10006
	s_lshl_b32 s21, s20, 7
	s_lshl_b32 s20, s20, 13
	s_add_u32 s20, s20, 0x30000
	s_add_u32 s22, s14, s20
	s_addc_u32 s23, s15, 0
	s_add_u32 s24, s22, 0x1000
	s_addc_u32 s25, s23, 0
	global_load_dwordx4 v[98:101], v210, s[22:23] offset:0
	global_load_dwordx4 v[102:105], v210, s[22:23] offset:1024
	global_load_dwordx4 v[106:109], v210, s[22:23] offset:2048
	global_load_dwordx4 v[110:113], v210, s[22:23] offset:3072
	global_load_dwordx4 v[114:117], v210, s[24:25] offset:0
	global_load_dwordx4 v[118:121], v210, s[24:25] offset:1024
	global_load_dwordx4 v[122:125], v210, s[24:25] offset:2048
	global_load_dwordx4 v[126:129], v210, s[24:25] offset:3072
	v_or_b32_e32 v250, s21, v230
	global_load_dwordx4 v[130:133], v250, s[4:5] offset:0
	global_load_dwordx4 v[134:137], v250, s[4:5] offset:32
	global_load_dwordx4 v[138:141], v250, s[4:5] offset:64
	global_load_dwordx4 v[142:145], v250, s[4:5] offset:96
	global_load_dwordx4 v[146:149], v250, s[6:7] offset:0
	global_load_dwordx4 v[150:153], v250, s[6:7] offset:32
	global_load_dwordx4 v[154:157], v250, s[6:7] offset:64
	global_load_dwordx4 v[158:161], v250, s[6:7] offset:96
	s_load_dword s26, s[8:9], 0x0
	v_mfma_f32_32x32x16_bf16 v[82:97], v[78:81], v[162:165], v[82:97]
	v_exp_f32_e32 v212, v36
	v_exp_f32_e32 v213, v40
	v_exp_f32_e32 v214, v44
	v_exp_f32_e32 v215, v48
	v_mfma_f32_32x32x16_bf16 v[82:97], v[74:77], v[166:169], v[82:97]
	v_exp_f32_e32 v217, v34
	v_fma_f32 v251, v212, s12, s12
	v_exp_f32_e32 v218, v38
	v_fma_f32 v252, v213, s12, s12
	v_exp_f32_e32 v219, v42
	v_fma_f32 v253, v214, s12, s12
	v_exp_f32_e32 v220, v46
	v_fma_f32 v254, v215, s12, s12
	v_mfma_f32_32x32x16_bf16 v[82:97], v[70:73], v[170:173], v[82:97]
	v_exp_f32_e32 v221, v35
	v_fmac_f32_e32 v251, v217, v251
	v_exp_f32_e32 v222, v39
	v_fmac_f32_e32 v252, v218, v252
	v_exp_f32_e32 v223, v43
	v_fmac_f32_e32 v253, v219, v253
	v_exp_f32_e32 v224, v47
	v_fmac_f32_e32 v254, v220, v254
	v_mfma_f32_32x32x16_bf16 v[82:97], v[66:69], v[174:177], v[82:97]
	v_rcp_f32_e32 v217, v251
	v_add_f32_e32 v221, 1.0, v221
	v_rcp_f32_e32 v218, v252
	v_add_f32_e32 v222, 1.0, v222
	v_rcp_f32_e32 v219, v253
	v_add_f32_e32 v223, 1.0, v223
	v_rcp_f32_e32 v220, v254
	v_add_f32_e32 v224, 1.0, v224
	v_mfma_f32_32x32x16_bf16 v[82:97], v[62:65], v[178:181], v[82:97]
	v_rcp_f32_e32 v221, v221
	v_fma_f32 v240, -v212, v217, v217
	v_rcp_f32_e32 v222, v222
	v_fma_f32 v241, -v213, v218, v218
	v_rcp_f32_e32 v223, v223
	v_fma_f32 v242, -v214, v219, v219
	v_rcp_f32_e32 v224, v224
	v_fma_f32 v243, -v215, v220, v220
	v_mfma_f32_32x32x16_bf16 v[82:97], v[58:61], v[182:185], v[82:97]
	v_exp_f32_e32 v246, v37
	v_fma_f32 v202, v221, v202, v240
	v_exp_f32_e32 v247, v41
	v_fma_f32 v203, v222, v203, v241
	v_exp_f32_e32 v248, v45
	v_fma_f32 v204, v223, v204, v242
	v_exp_f32_e32 v249, v49
	v_fma_f32 v205, v224, v205, v243
	v_mfma_f32_32x32x16_bf16 v[82:97], v[54:57], v[186:189], v[82:97]
	v_exp_f32_e32 v212, v202
	v_add_f32_e32 v246, 1.0, v246
	v_exp_f32_e32 v213, v203
	v_add_f32_e32 v247, 1.0, v247
	v_exp_f32_e32 v214, v204
	v_add_f32_e32 v248, 1.0, v248
	v_exp_f32_e32 v215, v205
	v_add_f32_e32 v249, 1.0, v249
	v_fmac_f32_e32 v246, v246, v212
	v_fmac_f32_e32 v247, v247, v213
	v_fmac_f32_e32 v248, v248, v214
	v_fmac_f32_e32 v249, v249, v215
	v_mfma_f32_32x32x16_bf16 v[82:97], v[50:53], v[190:193], v[82:97]
	v_rcp_f32_e32 v246, v246
	v_rcp_f32_e32 v247, v247
	v_rcp_f32_e32 v248, v248
	v_rcp_f32_e32 v249, v249
	v_fma_f32 v246, -v212, v246, v246
	v_fma_f32 v247, -v213, v247, v247
	v_fma_f32 v248, -v214, v248, v248
	v_fma_f32 v249, -v215, v249, v249
	v_cvt_pk_bf16_f32 v236, v246, v247
	v_cvt_pk_bf16_f32 v237, v248, v249
	s_waitcnt lgkmcnt(0)
	v_exp_f32_e32 v212, v84
	v_exp_f32_e32 v213, v88
	v_exp_f32_e32 v214, v92
	v_exp_f32_e32 v215, v96
	v_exp_f32_e32 v217, v82
	v_fma_f32 v251, v212, s12, s12
	v_exp_f32_e32 v218, v86
	v_fma_f32 v252, v213, s12, s12
	v_exp_f32_e32 v219, v90
	v_fma_f32 v253, v214, s12, s12
	v_exp_f32_e32 v220, v94
	v_fma_f32 v254, v215, s12, s12
	v_exp_f32_e32 v221, v83
	v_fmac_f32_e32 v251, v217, v251
	v_exp_f32_e32 v222, v87
	v_fmac_f32_e32 v252, v218, v252
	v_exp_f32_e32 v223, v91
	v_fmac_f32_e32 v253, v219, v253
	v_exp_f32_e32 v224, v95
	v_fmac_f32_e32 v254, v220, v254
	v_rcp_f32_e32 v217, v251
	v_add_f32_e32 v221, 1.0, v221
	v_rcp_f32_e32 v218, v252
	v_add_f32_e32 v222, 1.0, v222
	v_rcp_f32_e32 v219, v253
	v_add_f32_e32 v223, 1.0, v223
	v_rcp_f32_e32 v220, v254
	v_add_f32_e32 v224, 1.0, v224
	v_rcp_f32_e32 v221, v221
	v_fma_f32 v240, -v212, v217, v217
	v_rcp_f32_e32 v222, v222
	v_fma_f32 v241, -v213, v218, v218
	v_rcp_f32_e32 v223, v223
	v_fma_f32 v242, -v214, v219, v219
	v_rcp_f32_e32 v224, v224
	v_fma_f32 v243, -v215, v220, v220
	v_exp_f32_e32 v246, v85
	v_fma_f32 v206, v221, v206, v240
	v_exp_f32_e32 v247, v89
	v_fma_f32 v207, v222, v207, v241
	v_exp_f32_e32 v248, v93
	v_fma_f32 v208, v223, v208, v242
	v_exp_f32_e32 v249, v97
	v_fma_f32 v209, v224, v209, v243
	v_exp_f32_e32 v212, v206
	v_add_f32_e32 v246, 1.0, v246
	v_exp_f32_e32 v213, v207
	v_add_f32_e32 v247, 1.0, v247
	v_exp_f32_e32 v214, v208
	v_add_f32_e32 v248, 1.0, v248
	v_exp_f32_e32 v215, v209
	v_add_f32_e32 v249, 1.0, v249
	v_fmac_f32_e32 v246, v246, v212
	v_fmac_f32_e32 v247, v247, v213
	v_fmac_f32_e32 v248, v248, v214
	v_fmac_f32_e32 v249, v249, v215
	v_rcp_f32_e32 v246, v246
	v_rcp_f32_e32 v247, v247
	v_rcp_f32_e32 v248, v248
	v_rcp_f32_e32 v249, v249
	v_fma_f32 v246, -v212, v246, v246
	v_fma_f32 v247, -v213, v247, v247
	v_fma_f32 v248, -v214, v248, v248
	v_fma_f32 v249, -v215, v249, v249
	v_cvt_pk_bf16_f32 v238, v246, v247
	v_cvt_pk_bf16_f32 v239, v248, v249
	ds_write_b128 v211, v[236:239] offset:8192
	s_waitcnt lgkmcnt(0)
	s_barrier
	s_lshl_b32 s20, s19, 6
	s_and_b32 s20, s20, 0x2000
	v_or_b32_e32 v20, s20, v210
	ds_read_b128 v[162:165], v20 offset:0
	ds_read_b128 v[166:169], v20 offset:1024
	ds_read_b128 v[170:173], v20 offset:2048
	ds_read_b128 v[174:177], v20 offset:3072
	ds_read_b128 v[178:181], v20 offset:4096
	ds_read_b128 v[182:185], v20 offset:5120
	ds_read_b128 v[186:189], v20 offset:6144
	ds_read_b128 v[190:193], v20 offset:7168
	s_bfe_u32 s20, s19, 0x10006
	s_lshl_b32 s20, s20, 9
	s_and_b32 s21, s19, 0x80
	s_or_b32 s20, s20, s21
	v_lshlrev_b32_e32 v19, 2, v229
	v_add3_u32 v19, s20, v19, v228
	s_waitcnt vmcnt(0)
	s_waitcnt lgkmcnt(7)
	v_mfma_f32_32x32x16_bf16 v[2:17], v[98:101], v[162:165], 0
	s_waitcnt lgkmcnt(6)
	v_mfma_f32_32x32x16_bf16 v[2:17], v[102:105], v[166:169], v[2:17]
	s_waitcnt lgkmcnt(5)
	v_mfma_f32_32x32x16_bf16 v[2:17], v[106:109], v[170:173], v[2:17]
	s_waitcnt lgkmcnt(4)
	v_mfma_f32_32x32x16_bf16 v[2:17], v[110:113], v[174:177], v[2:17]
	s_waitcnt lgkmcnt(3)
	v_mfma_f32_32x32x16_bf16 v[2:17], v[114:117], v[178:181], v[2:17]
	s_waitcnt lgkmcnt(2)
	v_mfma_f32_32x32x16_bf16 v[2:17], v[118:121], v[182:185], v[2:17]
	s_waitcnt lgkmcnt(1)
	v_mfma_f32_32x32x16_bf16 v[2:17], v[122:125], v[186:189], v[2:17]
	s_waitcnt lgkmcnt(0)
	v_mfma_f32_32x32x16_bf16 v[2:17], v[126:129], v[190:193], v[2:17]
	s_nop 15
	s_nop 3
	v_add_f32_e32 v2, v2, v130
	v_add_f32_e32 v3, v3, v131
	v_add_f32_e32 v4, v4, v132
	v_add_f32_e32 v5, v5, v133
	v_add_f32_e32 v6, v6, v134
	v_add_f32_e32 v7, v7, v135
	v_add_f32_e32 v8, v8, v136
	v_add_f32_e32 v9, v9, v137
	v_add_f32_e32 v10, v10, v138
	v_add_f32_e32 v11, v11, v139
	v_add_f32_e32 v12, v12, v140
	v_add_f32_e32 v13, v13, v141
	v_add_f32_e32 v14, v14, v142
	v_add_f32_e32 v15, v15, v143
	v_add_f32_e32 v16, v16, v144
	v_add_f32_e32 v17, v17, v145
	v_max_f32_e32 v2, 0, v2
	v_max_f32_e32 v3, 0, v3
	v_max_f32_e32 v4, 0, v4
	v_max_f32_e32 v5, 0, v5
	v_max_f32_e32 v6, 0, v6
	v_max_f32_e32 v7, 0, v7
	v_max_f32_e32 v8, 0, v8
	v_max_f32_e32 v9, 0, v9
	v_max_f32_e32 v10, 0, v10
	v_max_f32_e32 v11, 0, v11
	v_max_f32_e32 v12, 0, v12
	v_max_f32_e32 v13, 0, v13
	v_max_f32_e32 v14, 0, v14
	v_max_f32_e32 v15, 0, v15
	v_max_f32_e32 v16, 0, v16
	v_max_f32_e32 v17, 0, v17
	v_fma_f32 v18, v2, v146, 0
	v_fmac_f32_e32 v18, v3, v147
	v_fmac_f32_e32 v18, v4, v148
	v_fmac_f32_e32 v18, v5, v149
	v_fmac_f32_e32 v18, v6, v150
	v_fmac_f32_e32 v18, v7, v151
	v_fmac_f32_e32 v18, v8, v152
	v_fmac_f32_e32 v18, v9, v153
	v_fmac_f32_e32 v18, v10, v154
	v_fmac_f32_e32 v18, v11, v155
	v_fmac_f32_e32 v18, v12, v156
	v_fmac_f32_e32 v18, v13, v157
	v_fmac_f32_e32 v18, v14, v158
	v_fmac_f32_e32 v18, v15, v159
	v_fmac_f32_e32 v18, v16, v160
	v_fmac_f32_e32 v18, v17, v161
	ds_write_b32 v19, v18 offset:35904
	s_branch .LBB1_40
